# nt11 + GEMM1 first-iteration waits skipped for units>=1 + GEMM3 pipelined epilogue loads and x-tile prefetch under the K-loop + P9b readlane hoist
# baseline (speedup 1.0000x reference)
;     __host__ __device__ bool next(int i, Unit& u) const {
;         const long L = (long)i * G + c; if (L >= nwg) return false;
;         int wgid = (int)L; { const int q = nwg / NXCD, r = nwg % NXCD, xcd = wgid % NXCD, off = wgid / NXCD; wgid = (xcd < r ? xcd * (q + 1) : r * (q + 1) + (xcd - r) * q) + off; }
;         const int nig = WGM * nN, gid = wgid / nig, fm = gid * WGM, gsz = (nM - fm) < WGM ? (nM - fm) : WGM;
;         u.pm = fm + ((wgid % nig) % gsz); u.pn = (wgid % nig) / gsz; return true;
;     }
.LBB0_176:
	s_add_i32 s81, s81, 1
	s_cmp_ge_u32 s81, 2
	s_cselect_b32 s98, 1, 0
	v_readlane_b32 s4, v255, 2
	s_mul_i32 s0, s81, s76
	s_mul_hi_u32 s1, s81, s4
	s_add_i32 s1, s1, s0
	s_mul_i32 s0, s81, s4
	s_add_u32 s4, s0, s2
	s_addc_u32 s5, s1, s77
	v_cmp_gt_i64_e32 vcc, s[4:5], v[208:209]
	v_cmp_lt_i64_e64 s[0:1], s[4:5], v[206:207]
	s_cbranch_vccnz .LBB0_178
	s_ashr_i32 s5, s4, 31
	s_lshr_b32 s5, s5, 29
	s_add_i32 s5, s4, s5
	s_ashr_i32 s26, s5, 3
	s_and_b32 s5, s5, -8
	s_sub_i32 s4, s4, s5
	s_cmp_lt_i32 s4, 0
	s_movk_i32 s5, 0x141
	s_cselect_b32 s5, s5, 0x140
	s_mul_i32 s4, s4, s5
	s_add_i32 s4, s4, s26
	s_mul_hi_i32 s5, s4, 0x66666667
	s_lshr_b32 s26, s5, 31
	s_ashr_i32 s5, s5, 8
	s_add_i32 s5, s5, s26
	s_lshl_b32 s26, s5, 3
	s_sub_i32 s27, 32, s26
	s_min_i32 s27, s27, 8
	s_abs_i32 s36, s27
	v_cvt_f32_u32_e32 v2, s36
	s_sub_i32 s38, 0, s36
	s_mulk_i32 s5, 0x280
	s_sub_i32 s4, s4, s5
	v_rcp_iflag_f32_e32 v2, v2
	s_abs_i32 s5, s4
	s_xor_b32 s37, s4, s27
	s_ashr_i32 s37, s37, 31
	v_mul_f32_e32 v2, 0x4f7ffffe, v2
	v_cvt_u32_f32_e32 v2, v2
	s_nop 0
	v_readfirstlane_b32 s39, v2
	s_mul_i32 s38, s38, s39
	s_mul_hi_u32 s38, s39, s38
	s_add_i32 s39, s39, s38
	s_mul_hi_u32 s38, s5, s39
	s_mul_i32 s39, s38, s36
	s_sub_i32 s5, s5, s39
	s_add_i32 s82, s38, 1
	s_sub_i32 s39, s5, s36
	s_cmp_ge_u32 s5, s36
	s_cselect_b32 s38, s82, s38
	s_cselect_b32 s5, s39, s5
	s_add_i32 s39, s38, 1
	s_cmp_ge_u32 s5, s36
	s_cselect_b32 s5, s39, s38
	s_xor_b32 s5, s5, s37
	s_sub_i32 s82, s5, s37
	s_mul_i32 s5, s82, s27
	s_sub_i32 s4, s4, s5
	s_add_i32 s83, s26, s4

.LBB0_181:
	ds_read_b128 v[158:161], v217
	ds_read_b128 v[154:157], v217 offset:1024
	ds_read_b128 v[150:153], v217 offset:2048
	ds_read_b128 v[146:149], v217 offset:3072
	ds_read_b128 v[118:121], v218
	ds_read_b128 v[106:109], v218 offset:1024
	ds_read_b128 v[102:105], v218 offset:2048
	ds_read_b128 v[98:101], v218 offset:3072
	s_mov_b32 m0, s73
	ds_read_b128 v[190:193], v219
	ds_read_b128 v[186:189], v219 offset:1024
	ds_read_b128 v[182:185], v219 offset:2048
	ds_read_b128 v[178:181], v219 offset:3072
	ds_read_b128 v[174:177], v219 offset:4096
	ds_read_b128 v[170:173], v219 offset:5120
	ds_read_b128 v[166:169], v219 offset:6144
	ds_read_b128 v[162:165], v219 offset:7168
	buffer_load_dwordx4 v1, s[20:23], s90 offen lds
	s_mov_b32 m0, s13
	s_mov_b64 s[4:5], -1
	buffer_load_dwordx4 v211, s[20:23], s90 offen lds
	s_and_b64 vcc, exec, s[38:39]
	s_cbranch_vccz .LBB0_183
	s_cmp_lg_u32 s98, 0
	s_cbranch_scc1 .Lw0_0
	s_waitcnt vmcnt(8)

; #define PG8_LAS __attribute__((address_space(3)))
; __device__ __forceinline__ void hook_issue(const TblHook& h, int it, int lane, PG8_LAS unsigned char* slot) {
;     const int q = __builtin_amdgcn_readfirstlane(it * h.ngw + h.gwave); const int qq = q < HK_NCHUNK ? q : 0; const bool isu = qq < HK_HALF; const int j = isu ? qq : qq - HK_HALF;
;     const __amdgpu_buffer_rsrc_t r = __builtin_amdgcn_make_buffer_rsrc((void*)(isu ? h.u : h.v), (short)0, 0x7fffffff, 0x00020000);
;     const unsigned so = (unsigned)j * 2048u, l16 = (unsigned)lane * 16u;
;     __builtin_amdgcn_raw_ptr_buffer_load_lds(r, (PG8_LAS void*)slot, 16, l16, so, 0, 0);
;     __builtin_amdgcn_raw_ptr_buffer_load_lds(r, (PG8_LAS void*)(slot + 1024), 16, l16, so + 1024u, 0, 0);
.LBB0_183:
	s_andn2_b64 vcc, exec, s[4:5]
	s_mul_i32 s40, s43, s42
	s_cbranch_vccnz .LBB0_185
	s_add_i32 s4, s40, s12
	s_cmp_lt_i32 s4, 0x40000
	s_cselect_b32 s41, s4, 0
	s_cmp_lt_i32 s41, 0x20000
	s_cselect_b64 s[26:27], -1, 0
	s_and_b64 s[4:5], s[26:27], exec
	s_cselect_b32 s4, s58, s60
	s_cselect_b32 s5, s59, s61
	s_lshl_b32 s41, s41, 11
	s_and_b32 s5, s5, 0xffff
	s_add_i32 s93, s41, 0xf0000000
	s_and_b64 s[26:27], s[26:27], exec
	s_mov_b32 m0, s74
	s_cselect_b32 s26, s41, s93
	buffer_load_dwordx4 v214, s[4:7], s26 offen lds
	s_bitset1_b32 s26, 10
	s_mov_b32 m0, s75
	s_nop 0
	buffer_load_dwordx4 v214, s[4:7], s26 offen lds
	s_cmp_lg_u32 s98, 0
	s_cbranch_scc1 .Lw0_1
	s_waitcnt vmcnt(10)
.Lw0_1:
.LBB0_185:
	s_add_i32 s4, s90, 0xfff7c080
	s_waitcnt lgkmcnt(0)
	s_cmp_eq_u32 s92, 28
	s_cselect_b32 s93, s88, s4
	s_cselect_b32 s41, s89, s91
	s_barrier
	s_setprio 1
	s_waitcnt lgkmcnt(7)
	v_mfma_i32_16x16x64_i8 v[142:145], v[158:161], v[190:193], v[142:145]
	s_waitcnt lgkmcnt(6)
	v_mfma_i32_16x16x64_i8 v[142:145], v[154:157], v[186:189], v[142:145]
	v_mfma_i32_16x16x64_i8 v[138:141], v[150:153], v[190:193], v[138:141]
	s_nop 0
	v_mfma_i32_16x16x64_i8 v[138:141], v[146:149], v[186:189], v[138:141]
	s_waitcnt lgkmcnt(5)
	v_mfma_i32_16x16x64_i8 v[126:129], v[158:161], v[182:185], v[126:129]
	s_waitcnt lgkmcnt(4)
	v_mfma_i32_16x16x64_i8 v[126:129], v[154:157], v[178:181], v[126:129]
	v_mfma_i32_16x16x64_i8 v[122:125], v[150:153], v[182:185], v[122:125]
	s_nop 0
	v_mfma_i32_16x16x64_i8 v[122:125], v[146:149], v[178:181], v[122:125]
	s_waitcnt lgkmcnt(3)
	v_mfma_i32_16x16x64_i8 v[94:97], v[158:161], v[174:177], v[94:97]
	s_waitcnt lgkmcnt(2)
	v_mfma_i32_16x16x64_i8 v[94:97], v[154:157], v[170:173], v[94:97]
	v_mfma_i32_16x16x64_i8 v[90:93], v[150:153], v[174:177], v[90:93]
	s_nop 0
	v_mfma_i32_16x16x64_i8 v[90:93], v[146:149], v[170:173], v[90:93]
	s_waitcnt lgkmcnt(1)
	v_mfma_i32_16x16x64_i8 v[78:81], v[158:161], v[166:169], v[78:81]
	s_waitcnt lgkmcnt(0)
	v_mfma_i32_16x16x64_i8 v[78:81], v[154:157], v[162:165], v[78:81]
	v_mfma_i32_16x16x64_i8 v[74:77], v[150:153], v[166:169], v[74:77]
	s_nop 0
	v_mfma_i32_16x16x64_i8 v[74:77], v[146:149], v[162:165], v[74:77]
	s_setprio 0
	s_setprio 1
	v_mfma_i32_16x16x64_i8 v[134:137], v[118:121], v[190:193], v[134:137]
	s_nop 0
	v_mfma_i32_16x16x64_i8 v[134:137], v[106:109], v[186:189], v[134:137]
	v_mfma_i32_16x16x64_i8 v[130:133], v[102:105], v[190:193], v[130:133]
	s_nop 0
	v_mfma_i32_16x16x64_i8 v[130:133], v[98:101], v[186:189], v[130:133]
	v_mfma_i32_16x16x64_i8 v[114:117], v[118:121], v[182:185], v[114:117]
	s_nop 0
	v_mfma_i32_16x16x64_i8 v[114:117], v[106:109], v[178:181], v[114:117]
	v_mfma_i32_16x16x64_i8 v[110:113], v[102:105], v[182:185], v[110:113]
	s_nop 0
	v_mfma_i32_16x16x64_i8 v[110:113], v[98:101], v[178:181], v[110:113]
	v_mfma_i32_16x16x64_i8 v[86:89], v[118:121], v[174:177], v[86:89]
	s_nop 0
	v_mfma_i32_16x16x64_i8 v[86:89], v[106:109], v[170:173], v[86:89]
	v_mfma_i32_16x16x64_i8 v[82:85], v[102:105], v[174:177], v[82:85]
	s_nop 0
	v_mfma_i32_16x16x64_i8 v[82:85], v[98:101], v[170:173], v[82:85]
	v_mfma_i32_16x16x64_i8 v[70:73], v[118:121], v[166:169], v[70:73]
	s_nop 0
	v_mfma_i32_16x16x64_i8 v[70:73], v[106:109], v[162:165], v[70:73]
	v_mfma_i32_16x16x64_i8 v[66:69], v[102:105], v[166:169], v[66:69]
	s_nop 0
	v_mfma_i32_16x16x64_i8 v[66:69], v[98:101], v[162:165], v[66:69]
	s_setprio 0
	s_barrier
	s_mov_b32 m0, s45
	s_mov_b32 s26, s22
	s_mov_b32 s27, s23
	ds_read_b128 v[190:193], v219 offset:16384
	ds_read_b128 v[186:189], v219 offset:17408
	ds_read_b128 v[182:185], v219 offset:18432
	ds_read_b128 v[178:181], v219 offset:19456
	ds_read_b128 v[174:177], v219 offset:20480
	ds_read_b128 v[170:173], v219 offset:21504
	ds_read_b128 v[166:169], v219 offset:22528
	ds_read_b128 v[162:165], v219 offset:23552
	buffer_load_dwordx4 v210, s[24:27], s41 offen lds
	s_mov_b32 m0, s46
	s_add_i32 s4, s41, 0x84000
	buffer_load_dwordx4 v212, s[24:27], s41 offen lds
	s_mov_b32 m0, s47
	s_and_b64 vcc, exec, s[38:39]
	buffer_load_dwordx4 v210, s[24:27], s4 offen lds
	s_mov_b32 m0, s48
	s_nop 0
	buffer_load_dwordx4 v212, s[24:27], s4 offen lds
	s_mov_b32 m0, s44
	s_mov_b64 s[4:5], -1
	buffer_load_dwordx4 v1, s[20:23], s93 offen lds
	s_mov_b32 m0, s49
	s_nop 0
	buffer_load_dwordx4 v211, s[20:23], s93 offen lds
	s_cbranch_vccz .LBB0_187
	s_cmp_lg_u32 s98, 0
	s_cbranch_scc1 .Lw0_2
	s_waitcnt vmcnt(8)

.LBB0_187:
	s_andn2_b64 vcc, exec, s[4:5]
	s_cbranch_vccnz .LBB0_189
	s_cmp_lg_u32 s98, 0
	s_cbranch_scc1 .Lw0_3
	s_waitcnt vmcnt(10)
.Lw0_3:
.LBB0_189:
	s_mov_b32 s98, 0
	s_waitcnt lgkmcnt(0)
	s_barrier
	s_setprio 1
	s_waitcnt lgkmcnt(7)
	v_mfma_i32_16x16x64_i8 v[62:65], v[158:161], v[190:193], v[62:65]
	s_waitcnt lgkmcnt(6)
	v_mfma_i32_16x16x64_i8 v[62:65], v[154:157], v[186:189], v[62:65]
	v_mfma_i32_16x16x64_i8 v[58:61], v[150:153], v[190:193], v[58:61]
	s_nop 0
	v_mfma_i32_16x16x64_i8 v[58:61], v[146:149], v[186:189], v[58:61]
	s_waitcnt lgkmcnt(5)
	v_mfma_i32_16x16x64_i8 v[46:49], v[158:161], v[182:185], v[46:49]
	s_waitcnt lgkmcnt(4)
	v_mfma_i32_16x16x64_i8 v[46:49], v[154:157], v[178:181], v[46:49]
	v_mfma_i32_16x16x64_i8 v[42:45], v[150:153], v[182:185], v[42:45]
	s_nop 0
	v_mfma_i32_16x16x64_i8 v[42:45], v[146:149], v[178:181], v[42:45]
	s_waitcnt lgkmcnt(3)
	v_mfma_i32_16x16x64_i8 v[30:33], v[158:161], v[174:177], v[30:33]
	s_waitcnt lgkmcnt(2)
	v_mfma_i32_16x16x64_i8 v[30:33], v[154:157], v[170:173], v[30:33]
	v_mfma_i32_16x16x64_i8 v[26:29], v[150:153], v[174:177], v[26:29]
	s_nop 0
	v_mfma_i32_16x16x64_i8 v[26:29], v[146:149], v[170:173], v[26:29]
	s_waitcnt lgkmcnt(1)
	v_mfma_i32_16x16x64_i8 v[14:17], v[158:161], v[166:169], v[14:17]
	s_waitcnt lgkmcnt(0)
	v_mfma_i32_16x16x64_i8 v[14:17], v[154:157], v[162:165], v[14:17]
	v_mfma_i32_16x16x64_i8 v[10:13], v[150:153], v[166:169], v[10:13]
	s_nop 0
	v_mfma_i32_16x16x64_i8 v[10:13], v[146:149], v[162:165], v[10:13]
	s_setprio 0
	s_setprio 1
	v_mfma_i32_16x16x64_i8 v[54:57], v[118:121], v[190:193], v[54:57]
	s_nop 0
	v_mfma_i32_16x16x64_i8 v[54:57], v[106:109], v[186:189], v[54:57]
	v_mfma_i32_16x16x64_i8 v[50:53], v[102:105], v[190:193], v[50:53]
	s_nop 0
	v_mfma_i32_16x16x64_i8 v[50:53], v[98:101], v[186:189], v[50:53]
	v_mfma_i32_16x16x64_i8 v[38:41], v[118:121], v[182:185], v[38:41]
	s_nop 0
	v_mfma_i32_16x16x64_i8 v[38:41], v[106:109], v[178:181], v[38:41]
	v_mfma_i32_16x16x64_i8 v[34:37], v[102:105], v[182:185], v[34:37]
	s_nop 0
	v_mfma_i32_16x16x64_i8 v[34:37], v[98:101], v[178:181], v[34:37]
	v_mfma_i32_16x16x64_i8 v[22:25], v[118:121], v[174:177], v[22:25]
	s_nop 0
	v_mfma_i32_16x16x64_i8 v[22:25], v[106:109], v[170:173], v[22:25]
	v_mfma_i32_16x16x64_i8 v[18:21], v[102:105], v[174:177], v[18:21]
	s_nop 0
	v_mfma_i32_16x16x64_i8 v[18:21], v[98:101], v[170:173], v[18:21]
	v_mfma_i32_16x16x64_i8 v[6:9], v[118:121], v[166:169], v[6:9]
	s_nop 0
	v_mfma_i32_16x16x64_i8 v[6:9], v[106:109], v[162:165], v[6:9]
	v_mfma_i32_16x16x64_i8 v[2:5], v[102:105], v[166:169], v[2:5]
	s_nop 0
	v_mfma_i32_16x16x64_i8 v[2:5], v[98:101], v[162:165], v[2:5]
	s_setprio 0
	s_barrier
	v_add_u32_e32 v98, 0x18000, v216
	ds_read_b128 v[158:161], v98
	ds_read_b128 v[154:157], v98 offset:1024
	ds_read_b128 v[150:153], v98 offset:2048
	ds_read_b128 v[146:149], v98 offset:3072
	v_add_u32_e32 v98, 0x1c000, v216
	ds_read_b128 v[118:121], v98
	ds_read_b128 v[106:109], v98 offset:1024
	ds_read_b128 v[102:105], v98 offset:2048
	ds_read_b128 v[98:101], v98 offset:3072
	s_mov_b32 m0, s50
	s_add_i32 s4, s93, 0x84000
	ds_read_b128 v[190:193], v219 offset:32768
	ds_read_b128 v[186:189], v219 offset:33792
	ds_read_b128 v[182:185], v219 offset:34816
	ds_read_b128 v[178:181], v219 offset:35840
	ds_read_b128 v[174:177], v219 offset:36864
	ds_read_b128 v[170:173], v219 offset:37888
	ds_read_b128 v[166:169], v219 offset:38912
	ds_read_b128 v[162:165], v219 offset:39936
	buffer_load_dwordx4 v1, s[20:23], s4 offen lds
	s_mov_b32 m0, s51
	s_and_b64 vcc, exec, s[38:39]
	buffer_load_dwordx4 v211, s[20:23], s4 offen lds
	s_mov_b64 s[4:5], -1
	s_cbranch_vccz .LBB0_191
	s_waitcnt vmcnt(8)
	s_mov_b64 s[4:5], 0

;     __host__ __device__ bool next(int i, Unit& u) const {
;         const long L = (long)i * G + c; if (L >= nwg) return false;
;         int wgid = (int)L; { const int q = nwg / NXCD, r = nwg % NXCD, xcd = wgid % NXCD, off = wgid / NXCD; wgid = (xcd < r ? xcd * (q + 1) : r * (q + 1) + (xcd - r) * q) + off; }
;         const int nig = WGM * nN, gid = wgid / nig, fm = gid * WGM, gsz = (nM - fm) < WGM ? (nM - fm) : WGM;
;         u.pm = fm + ((wgid % nig) % gsz); u.pn = (wgid % nig) / gsz; return true;
;     }
.LBB0_607:
	s_lshl_b32 s78, s29, 22
	s_lshl_b32 s79, s28, 10
	s_add_u32 s78, s78, s79
	v_readlane_b32 s79, v255, 10
	s_lshl_b32 s79, s79, 19
	s_add_u32 s78, s78, s79
	s_add_u32 s78, s8, s78
	s_addc_u32 s79, s9, 0
	v_bfe_u32 v253, v202, 3, 1
	v_and_b32_e32 v254, 7, v202
	v_lshlrev_b32_e32 v253, 14, v253
	v_lshl_or_b32 v253, v254, 7, v253
	s_add_i32 s37, s37, 1
	v_readlane_b32 s22, v255, 2
	s_mul_i32 s4, s37, s46
	s_mul_hi_u32 s5, s37, s22
	s_add_i32 s5, s5, s4
	s_mul_i32 s4, s37, s22
	s_add_u32 s22, s4, s2
	s_addc_u32 s23, s5, s47
	v_cmp_gt_i64_e32 vcc, s[22:23], v[164:165]
	v_cmp_lt_i64_e64 s[4:5], s[22:23], v[162:163]
	s_cbranch_vccnz .LBB0_613
	s_ashr_i32 s23, s22, 31
	s_lshr_b32 s23, s23, 29
	s_add_i32 s58, s22, s23
	s_and_b32 s23, s58, -8
	s_sub_i32 s59, s22, s23
	s_cmp_gt_i32 s59, -1
	s_mov_b64 s[22:23], -1
	s_cbranch_scc0 .LBB0_610
	s_lshl_b32 s60, s59, 6
	s_mov_b64 s[22:23], 0

.LBB0_614:
	ds_read_b128 v[158:161], v171
	ds_read_b128 v[154:157], v171 offset:1024
	ds_read_b128 v[150:153], v171 offset:2048
	ds_read_b128 v[146:149], v171 offset:3072
	ds_read_b128 v[142:145], v172
	ds_read_b128 v[138:141], v172 offset:1024
	ds_read_b128 v[74:77], v172 offset:2048
	ds_read_b128 v[66:69], v172 offset:3072
	s_add_i32 s22, s70, 0xfff7c080
	s_cmp_eq_u32 s72, 28
	s_cselect_b32 s75, s68, s22
	s_cselect_b32 s74, s69, s71
	s_or_b32 s73, s75, 0x80
	s_mov_b32 m0, s44
	ds_read_b128 v[178:181], v173
	ds_read_b128 v[182:185], v173 offset:1024
	ds_read_b128 v[186:189], v173 offset:2048
	ds_read_b128 v[190:193], v173 offset:3072
	ds_read_b128 v[194:197], v173 offset:4096
	ds_read_b128 v[198:201], v173 offset:5120
	ds_read_b128 v[204:207], v173 offset:6144
	ds_read_b128 v[208:211], v173 offset:7168
	buffer_load_dwordx4 v1, s[16:19], s70 offen lds
	s_mov_b32 m0, s45
	s_nop 0
	buffer_load_dwordx4 v167, s[16:19], s70 offen lds
	s_waitcnt vmcnt(8)
	s_waitcnt lgkmcnt(0)
	s_barrier
	s_setprio 1
	s_waitcnt lgkmcnt(7)
	v_mfma_i32_16x16x64_i8 v[62:65], v[158:161], v[178:181], v[62:65]
	s_waitcnt lgkmcnt(6)
	v_mfma_i32_16x16x64_i8 v[62:65], v[154:157], v[182:185], v[62:65]
	v_mfma_i32_16x16x64_i8 v[50:53], v[150:153], v[178:181], v[50:53]
	s_nop 0
	v_mfma_i32_16x16x64_i8 v[50:53], v[146:149], v[182:185], v[50:53]
	s_waitcnt lgkmcnt(5)
	v_mfma_i32_16x16x64_i8 v[126:129], v[158:161], v[186:189], v[126:129]
	s_waitcnt lgkmcnt(4)
	v_mfma_i32_16x16x64_i8 v[126:129], v[154:157], v[190:193], v[126:129]
	v_mfma_i32_16x16x64_i8 v[122:125], v[150:153], v[186:189], v[122:125]
	s_nop 0
	v_mfma_i32_16x16x64_i8 v[122:125], v[146:149], v[190:193], v[122:125]
	s_waitcnt lgkmcnt(3)
	v_mfma_i32_16x16x64_i8 v[110:113], v[158:161], v[194:197], v[110:113]
	s_waitcnt lgkmcnt(2)
	v_mfma_i32_16x16x64_i8 v[110:113], v[154:157], v[198:201], v[110:113]
	v_mfma_i32_16x16x64_i8 v[106:109], v[150:153], v[194:197], v[106:109]
	s_nop 0
	v_mfma_i32_16x16x64_i8 v[106:109], v[146:149], v[198:201], v[106:109]
	s_waitcnt lgkmcnt(1)
	v_mfma_i32_16x16x64_i8 v[94:97], v[158:161], v[204:207], v[94:97]
	s_waitcnt lgkmcnt(0)
	v_mfma_i32_16x16x64_i8 v[94:97], v[154:157], v[208:211], v[94:97]
	v_mfma_i32_16x16x64_i8 v[90:93], v[150:153], v[204:207], v[90:93]
	s_nop 0
	v_mfma_i32_16x16x64_i8 v[90:93], v[146:149], v[208:211], v[90:93]
	s_setprio 0
	s_setprio 1
	v_mfma_i32_16x16x64_i8 v[134:137], v[142:145], v[178:181], v[134:137]
	s_nop 0
	v_mfma_i32_16x16x64_i8 v[134:137], v[138:141], v[182:185], v[134:137]
	v_mfma_i32_16x16x64_i8 v[130:133], v[74:77], v[178:181], v[130:133]
	s_nop 0
	v_mfma_i32_16x16x64_i8 v[130:133], v[66:69], v[182:185], v[130:133]
	v_mfma_i32_16x16x64_i8 v[118:121], v[142:145], v[186:189], v[118:121]
	s_nop 0
	v_mfma_i32_16x16x64_i8 v[118:121], v[138:141], v[190:193], v[118:121]
	v_mfma_i32_16x16x64_i8 v[114:117], v[74:77], v[186:189], v[114:117]
	s_nop 0
	v_mfma_i32_16x16x64_i8 v[114:117], v[66:69], v[190:193], v[114:117]
	v_mfma_i32_16x16x64_i8 v[102:105], v[142:145], v[194:197], v[102:105]
	s_nop 0
	v_mfma_i32_16x16x64_i8 v[102:105], v[138:141], v[198:201], v[102:105]
	v_mfma_i32_16x16x64_i8 v[98:101], v[74:77], v[194:197], v[98:101]
	s_nop 0
	v_mfma_i32_16x16x64_i8 v[98:101], v[66:69], v[198:201], v[98:101]
	v_mfma_i32_16x16x64_i8 v[86:89], v[142:145], v[204:207], v[86:89]
	s_nop 0
	v_mfma_i32_16x16x64_i8 v[86:89], v[138:141], v[208:211], v[86:89]
	v_mfma_i32_16x16x64_i8 v[82:85], v[74:77], v[204:207], v[82:85]
	s_nop 0
	v_mfma_i32_16x16x64_i8 v[82:85], v[66:69], v[208:211], v[82:85]
	s_setprio 0
	s_barrier
	s_mov_b32 m0, s27
	s_mov_b32 s22, s18
	s_mov_b32 s23, s19
	ds_read_b128 v[178:181], v173 offset:16384
	ds_read_b128 v[182:185], v173 offset:17408
	ds_read_b128 v[186:189], v173 offset:18432
	ds_read_b128 v[190:193], v173 offset:19456
	ds_read_b128 v[194:197], v173 offset:20480
	ds_read_b128 v[198:201], v173 offset:21504
	ds_read_b128 v[204:207], v173 offset:22528
	ds_read_b128 v[208:211], v173 offset:23552
	buffer_load_dwordx4 v166, s[20:23], s74 offen lds
	s_mov_b32 m0, s30
	s_add_i32 s76, s74, 0x84000
	buffer_load_dwordx4 v168, s[20:23], s74 offen lds
	s_mov_b32 m0, s31
	s_nop 0
	buffer_load_dwordx4 v166, s[20:23], s76 offen lds
	s_mov_b32 m0, s33
	s_nop 0
	buffer_load_dwordx4 v168, s[20:23], s76 offen lds
	s_mov_b32 m0, s13
	s_nop 0
	buffer_load_dwordx4 v1, s[16:19], s75 offen lds
	s_mov_b32 m0, s34
	s_nop 0
	buffer_load_dwordx4 v167, s[16:19], s75 offen lds
	global_load_dword v254, v253, s[78:79]
	s_add_u32 s78, s78, 0x8000
	s_addc_u32 s79, s79, 0
	s_waitcnt vmcnt(9)
	s_waitcnt lgkmcnt(0)
	s_barrier
	s_setprio 1
	s_waitcnt lgkmcnt(7)
	v_mfma_i32_16x16x64_i8 v[78:81], v[158:161], v[178:181], v[78:81]
	s_waitcnt lgkmcnt(6)
	v_mfma_i32_16x16x64_i8 v[78:81], v[154:157], v[182:185], v[78:81]
	v_mfma_i32_16x16x64_i8 v[70:73], v[150:153], v[178:181], v[70:73]
	s_nop 0
	v_mfma_i32_16x16x64_i8 v[70:73], v[146:149], v[182:185], v[70:73]
	s_waitcnt lgkmcnt(5)
	v_mfma_i32_16x16x64_i8 v[46:49], v[158:161], v[186:189], v[46:49]
	s_waitcnt lgkmcnt(4)
	v_mfma_i32_16x16x64_i8 v[46:49], v[154:157], v[190:193], v[46:49]
	v_mfma_i32_16x16x64_i8 v[42:45], v[150:153], v[186:189], v[42:45]
	s_nop 0
	v_mfma_i32_16x16x64_i8 v[42:45], v[146:149], v[190:193], v[42:45]
	s_waitcnt lgkmcnt(3)
	v_mfma_i32_16x16x64_i8 v[30:33], v[158:161], v[194:197], v[30:33]
	s_waitcnt lgkmcnt(2)
	v_mfma_i32_16x16x64_i8 v[30:33], v[154:157], v[198:201], v[30:33]
	v_mfma_i32_16x16x64_i8 v[26:29], v[150:153], v[194:197], v[26:29]
	s_nop 0
	v_mfma_i32_16x16x64_i8 v[26:29], v[146:149], v[198:201], v[26:29]
	s_waitcnt lgkmcnt(1)
	v_mfma_i32_16x16x64_i8 v[14:17], v[158:161], v[204:207], v[14:17]
	s_waitcnt lgkmcnt(0)
	v_mfma_i32_16x16x64_i8 v[14:17], v[154:157], v[208:211], v[14:17]
	v_mfma_i32_16x16x64_i8 v[10:13], v[150:153], v[204:207], v[10:13]
	s_nop 0
	v_mfma_i32_16x16x64_i8 v[10:13], v[146:149], v[208:211], v[10:13]
	s_setprio 0
	s_setprio 1
	v_mfma_i32_16x16x64_i8 v[58:61], v[142:145], v[178:181], v[58:61]
	s_nop 0
	v_mfma_i32_16x16x64_i8 v[58:61], v[138:141], v[182:185], v[58:61]
	v_mfma_i32_16x16x64_i8 v[54:57], v[74:77], v[178:181], v[54:57]
	s_nop 0
	v_mfma_i32_16x16x64_i8 v[54:57], v[66:69], v[182:185], v[54:57]
	v_mfma_i32_16x16x64_i8 v[38:41], v[142:145], v[186:189], v[38:41]
	s_nop 0
	v_mfma_i32_16x16x64_i8 v[38:41], v[138:141], v[190:193], v[38:41]
	v_mfma_i32_16x16x64_i8 v[34:37], v[74:77], v[186:189], v[34:37]
	s_nop 0
	v_mfma_i32_16x16x64_i8 v[34:37], v[66:69], v[190:193], v[34:37]
	v_mfma_i32_16x16x64_i8 v[22:25], v[142:145], v[194:197], v[22:25]
	s_nop 0
	v_mfma_i32_16x16x64_i8 v[22:25], v[138:141], v[198:201], v[22:25]
	v_mfma_i32_16x16x64_i8 v[18:21], v[74:77], v[194:197], v[18:21]
	s_nop 0
	v_mfma_i32_16x16x64_i8 v[18:21], v[66:69], v[198:201], v[18:21]
	v_mfma_i32_16x16x64_i8 v[6:9], v[142:145], v[204:207], v[6:9]
	s_nop 0
	v_mfma_i32_16x16x64_i8 v[6:9], v[138:141], v[208:211], v[6:9]
	v_mfma_i32_16x16x64_i8 v[2:5], v[74:77], v[204:207], v[2:5]
	s_nop 0
	v_mfma_i32_16x16x64_i8 v[2:5], v[66:69], v[208:211], v[2:5]
	s_setprio 0
	s_barrier
	ds_read_b128 v[66:69], v174
	ds_read_b128 v[74:77], v174 offset:1024
	ds_read_b128 v[138:141], v174 offset:2048
	ds_read_b128 v[142:145], v174 offset:3072
	ds_read_b128 v[146:149], v175
	ds_read_b128 v[150:153], v175 offset:1024
	ds_read_b128 v[154:157], v175 offset:2048
	ds_read_b128 v[158:161], v175 offset:3072
	s_add_i32 s75, s75, 0x84000
	s_mov_b32 m0, s35
	ds_read_b128 v[178:181], v173 offset:32768
	ds_read_b128 v[182:185], v173 offset:33792
	ds_read_b128 v[186:189], v173 offset:34816
	ds_read_b128 v[190:193], v173 offset:35840
	ds_read_b128 v[194:197], v173 offset:36864
	ds_read_b128 v[198:201], v173 offset:37888
	ds_read_b128 v[204:207], v173 offset:38912
	ds_read_b128 v[208:211], v173 offset:39936
	buffer_load_dwordx4 v1, s[16:19], s75 offen lds
	s_mov_b32 m0, s36
	s_nop 0
	buffer_load_dwordx4 v167, s[16:19], s75 offen lds
	s_waitcnt vmcnt(9)
	s_waitcnt lgkmcnt(0)
	s_barrier
	s_setprio 1
	s_waitcnt lgkmcnt(7)
	v_mfma_i32_16x16x64_i8 v[62:65], v[66:69], v[178:181], v[62:65]
	s_waitcnt lgkmcnt(6)
	v_mfma_i32_16x16x64_i8 v[62:65], v[74:77], v[182:185], v[62:65]
	v_mfma_i32_16x16x64_i8 v[50:53], v[138:141], v[178:181], v[50:53]
	s_nop 0
	v_mfma_i32_16x16x64_i8 v[50:53], v[142:145], v[182:185], v[50:53]
	s_waitcnt lgkmcnt(5)
	v_mfma_i32_16x16x64_i8 v[126:129], v[66:69], v[186:189], v[126:129]
	s_waitcnt lgkmcnt(4)
	v_mfma_i32_16x16x64_i8 v[126:129], v[74:77], v[190:193], v[126:129]
	v_mfma_i32_16x16x64_i8 v[122:125], v[138:141], v[186:189], v[122:125]
	s_nop 0
	v_mfma_i32_16x16x64_i8 v[122:125], v[142:145], v[190:193], v[122:125]
	s_waitcnt lgkmcnt(3)
	v_mfma_i32_16x16x64_i8 v[110:113], v[66:69], v[194:197], v[110:113]
	s_waitcnt lgkmcnt(2)
	v_mfma_i32_16x16x64_i8 v[110:113], v[74:77], v[198:201], v[110:113]
	v_mfma_i32_16x16x64_i8 v[106:109], v[138:141], v[194:197], v[106:109]
	s_nop 0
	v_mfma_i32_16x16x64_i8 v[106:109], v[142:145], v[198:201], v[106:109]
	s_waitcnt lgkmcnt(1)
	v_mfma_i32_16x16x64_i8 v[94:97], v[66:69], v[204:207], v[94:97]
	s_waitcnt lgkmcnt(0)
	v_mfma_i32_16x16x64_i8 v[94:97], v[74:77], v[208:211], v[94:97]
	v_mfma_i32_16x16x64_i8 v[90:93], v[138:141], v[204:207], v[90:93]
	s_nop 0
	v_mfma_i32_16x16x64_i8 v[90:93], v[142:145], v[208:211], v[90:93]
	s_setprio 0
	s_setprio 1
	v_mfma_i32_16x16x64_i8 v[134:137], v[146:149], v[178:181], v[134:137]
	s_nop 0
	v_mfma_i32_16x16x64_i8 v[134:137], v[150:153], v[182:185], v[134:137]
	v_mfma_i32_16x16x64_i8 v[130:133], v[154:157], v[178:181], v[130:133]
	s_nop 0
	v_mfma_i32_16x16x64_i8 v[130:133], v[158:161], v[182:185], v[130:133]
	v_mfma_i32_16x16x64_i8 v[118:121], v[146:149], v[186:189], v[118:121]
	s_nop 0
	v_mfma_i32_16x16x64_i8 v[118:121], v[150:153], v[190:193], v[118:121]
	v_mfma_i32_16x16x64_i8 v[114:117], v[154:157], v[186:189], v[114:117]
	s_nop 0
	v_mfma_i32_16x16x64_i8 v[114:117], v[158:161], v[190:193], v[114:117]
	v_mfma_i32_16x16x64_i8 v[102:105], v[146:149], v[194:197], v[102:105]
	s_nop 0
	v_mfma_i32_16x16x64_i8 v[102:105], v[150:153], v[198:201], v[102:105]
	v_mfma_i32_16x16x64_i8 v[98:101], v[154:157], v[194:197], v[98:101]
	s_nop 0
	v_mfma_i32_16x16x64_i8 v[98:101], v[158:161], v[198:201], v[98:101]
	v_mfma_i32_16x16x64_i8 v[86:89], v[146:149], v[204:207], v[86:89]
	s_nop 0
	v_mfma_i32_16x16x64_i8 v[86:89], v[150:153], v[208:211], v[86:89]
	v_mfma_i32_16x16x64_i8 v[82:85], v[154:157], v[204:207], v[82:85]
	s_nop 0
	v_mfma_i32_16x16x64_i8 v[82:85], v[158:161], v[208:211], v[82:85]
	s_setprio 0
	s_barrier
;     __device__ __forceinline__ void operator()(const f32x4 (&acc)[2][2][4][2], const Unit& u, int wr, int wc, int fr, int fq) const {
;         const int row0 = u.pm * BM + wr * 64 + fr, col0 = u.pn * BM + wc * 32 + 8 * fq;
;         typedef unsigned u32x2e __attribute__((ext_vector_type(2)));
;         f32x4 gv[2][2];
; #pragma unroll
;         for (int bj = 0; bj < 2; ++bj)
; #pragma unroll
;             for (int n = 0; n < 2; ++n) gv[bj][n] = *(const f32x4*)(gain + col0 + bj * HALF + 4 * n);
;         float* SSQP = (float*)(ws + OFF_SSQP); unsigned char* Q8 = ws + OFF_Q8;
; #pragma unroll
;         for (int ai = 0; ai < 2; ++ai)
; #pragma unroll
;             for (int m = 0; m < 4; ++m) { const size_t r = (size_t)(row0 + ai * HALF + m * 16); float ss = 0.f;
; #pragma unroll
;                 for (int bj = 0; bj < 2; ++bj) { const size_t off = r * 4096 + col0 + bj * HALF;
;                     const f32x4 v0 = acc[ai][bj][m][0] * scale + *(const f32x4*)(R + off), v1 = acc[ai][bj][m][1] * scale + *(const f32x4*)(R + off + 4);
	s_mov_b32 m0, s38
	s_or_b32 s75, s74, 0x80
	ds_read_b128 v[178:181], v173 offset:49152
	ds_read_b128 v[182:185], v173 offset:50176
	ds_read_b128 v[186:189], v173 offset:51200
	ds_read_b128 v[190:193], v173 offset:52224
	ds_read_b128 v[194:197], v173 offset:53248
	ds_read_b128 v[198:201], v173 offset:54272
	ds_read_b128 v[204:207], v173 offset:55296
	ds_read_b128 v[208:211], v173 offset:56320
	buffer_load_dwordx4 v166, s[20:23], s75 offen lds
	s_mov_b32 m0, s39
	s_add_i32 s74, s74, 0x84080
	buffer_load_dwordx4 v168, s[20:23], s75 offen lds
	s_mov_b32 m0, s42
	s_nop 0
	buffer_load_dwordx4 v166, s[20:23], s74 offen lds
	s_mov_b32 m0, s43
	s_nop 0
	buffer_load_dwordx4 v168, s[20:23], s74 offen lds
	s_mov_b32 m0, s40
	s_nop 0
	buffer_load_dwordx4 v1, s[16:19], s73 offen lds
	s_mov_b32 m0, s41
	s_nop 0
	buffer_load_dwordx4 v167, s[16:19], s73 offen lds
	s_waitcnt vmcnt(9)
	s_waitcnt lgkmcnt(0)
	s_barrier
	s_setprio 1
	s_waitcnt lgkmcnt(7)
	v_mfma_i32_16x16x64_i8 v[78:81], v[66:69], v[178:181], v[78:81]
	s_waitcnt lgkmcnt(6)
	v_mfma_i32_16x16x64_i8 v[78:81], v[74:77], v[182:185], v[78:81]
	v_mfma_i32_16x16x64_i8 v[70:73], v[138:141], v[178:181], v[70:73]
	s_nop 0
	v_mfma_i32_16x16x64_i8 v[70:73], v[142:145], v[182:185], v[70:73]
	s_waitcnt lgkmcnt(5)
	v_mfma_i32_16x16x64_i8 v[46:49], v[66:69], v[186:189], v[46:49]
	s_waitcnt lgkmcnt(4)
	v_mfma_i32_16x16x64_i8 v[46:49], v[74:77], v[190:193], v[46:49]
	v_mfma_i32_16x16x64_i8 v[42:45], v[138:141], v[186:189], v[42:45]
	s_nop 0
	v_mfma_i32_16x16x64_i8 v[42:45], v[142:145], v[190:193], v[42:45]
	s_waitcnt lgkmcnt(3)
	v_mfma_i32_16x16x64_i8 v[30:33], v[66:69], v[194:197], v[30:33]
	s_waitcnt lgkmcnt(2)
	v_mfma_i32_16x16x64_i8 v[30:33], v[74:77], v[198:201], v[30:33]
	v_mfma_i32_16x16x64_i8 v[26:29], v[138:141], v[194:197], v[26:29]
	s_nop 0
	v_mfma_i32_16x16x64_i8 v[26:29], v[142:145], v[198:201], v[26:29]
	s_waitcnt lgkmcnt(1)
	v_mfma_i32_16x16x64_i8 v[14:17], v[66:69], v[204:207], v[14:17]
	s_waitcnt lgkmcnt(0)
	v_mfma_i32_16x16x64_i8 v[14:17], v[74:77], v[208:211], v[14:17]
	v_mfma_i32_16x16x64_i8 v[10:13], v[138:141], v[204:207], v[10:13]
	s_nop 0
	v_mfma_i32_16x16x64_i8 v[10:13], v[142:145], v[208:211], v[10:13]
	s_setprio 0
	s_setprio 1
	v_mfma_i32_16x16x64_i8 v[58:61], v[146:149], v[178:181], v[58:61]
	s_nop 0
	v_mfma_i32_16x16x64_i8 v[58:61], v[150:153], v[182:185], v[58:61]
	v_mfma_i32_16x16x64_i8 v[54:57], v[154:157], v[178:181], v[54:57]
	s_nop 0
	v_mfma_i32_16x16x64_i8 v[54:57], v[158:161], v[182:185], v[54:57]
	v_mfma_i32_16x16x64_i8 v[38:41], v[146:149], v[186:189], v[38:41]
	s_nop 0
	v_mfma_i32_16x16x64_i8 v[38:41], v[150:153], v[190:193], v[38:41]
	v_mfma_i32_16x16x64_i8 v[34:37], v[154:157], v[186:189], v[34:37]
	s_nop 0
	v_mfma_i32_16x16x64_i8 v[34:37], v[158:161], v[190:193], v[34:37]
	v_mfma_i32_16x16x64_i8 v[22:25], v[146:149], v[194:197], v[22:25]
	s_nop 0
	v_mfma_i32_16x16x64_i8 v[22:25], v[150:153], v[198:201], v[22:25]
	v_mfma_i32_16x16x64_i8 v[18:21], v[154:157], v[194:197], v[18:21]
	s_nop 0
	v_mfma_i32_16x16x64_i8 v[18:21], v[158:161], v[198:201], v[18:21]
	v_mfma_i32_16x16x64_i8 v[6:9], v[146:149], v[204:207], v[6:9]
	s_nop 0
	v_mfma_i32_16x16x64_i8 v[6:9], v[150:153], v[208:211], v[6:9]
	v_mfma_i32_16x16x64_i8 v[2:5], v[154:157], v[204:207], v[2:5]
	s_nop 0
	v_mfma_i32_16x16x64_i8 v[2:5], v[158:161], v[208:211], v[2:5]
	s_setprio 0
	s_barrier
	s_add_i32 s72, s72, 2
	s_addk_i32 s70, 0x100
	s_addk_i32 s71, 0x100
	s_cmp_gt_u32 s72, 29
	s_cbranch_scc0 .LBB0_614
	s_nop 7
	s_nop 7
	s_nop 7
	s_and_b64 vcc, exec, s[24:25]
	s_cbranch_vccz .LBB0_617
	s_barrier
.LBB0_617:
	v_lshl_add_u32 v140, s29, 8, v169
	v_lshl_or_b32 v138, s28, 8, v170
	v_ashrrev_i32_e32 v141, 31, v140
	v_ashrrev_i32_e32 v139, 31, v138
	v_lshlrev_b64 v[66:67], 12, v[140:141]
	v_lshl_add_u64 v[154:155], v[66:67], 0, v[138:139]
	v_lshl_add_u64 v[156:157], v[154:155], 2, s[8:9]
	global_load_dwordx4 v[146:149], v[156:157], off nt
	global_load_dwordx4 v[150:153], v[156:157], off offset:16 nt
	v_lshlrev_b32_e32 v252, 2, v154
	global_load_dwordx4 v[244:247], v252, s[8:9] offset:512
	global_load_dwordx4 v[248:251], v252, s[8:9] offset:528
	v_lshl_add_u64 v[144:145], v[138:139], 2, s[52:53]
	global_load_dwordx4 v[74:77], v[144:145], off
	global_load_dwordx4 v[66:69], v[144:145], off offset:16
	v_cvt_f32_i32_e32 v159, v63
	v_cvt_f32_i32_e32 v158, v62
	v_cvt_f32_i32_e32 v161, v65
	v_cvt_f32_i32_e32 v160, v64
	v_cvt_f32_i32_e32 v179, v51
	v_cvt_f32_i32_e32 v178, v50
	v_cvt_f32_i32_e32 v181, v53
	v_cvt_f32_i32_e32 v180, v52
	v_lshlrev_b64 v[154:155], 1, v[154:155]
	global_load_dwordx4 v[50:53], v[144:145], off offset:528
	global_load_dwordx4 v[62:65], v[144:145], off offset:512
	s_add_u32 s98, s8, 0x40000
	s_addc_u32 s99, s9, 0
	global_load_dwordx4 v[212:215], v252, s[98:99]
	global_load_dwordx4 v[216:219], v252, s[98:99] offset:16
	global_load_dwordx4 v[220:223], v252, s[98:99] offset:512
	global_load_dwordx4 v[224:227], v252, s[98:99] offset:528
	v_lshl_add_u64 v[182:183], s[14:15], 0, v[154:155]
	v_readlane_b32 s22, v255, 13
	v_readlane_b32 s23, v255, 14
	v_cvt_f32_i32_e32 v135, v135
	v_cvt_f32_i32_e32 v134, v134
	v_lshl_add_u64 v[142:143], s[22:23], 0, v[138:139]
	v_mad_i64_i32 v[144:145], s[22:23], v140, s50, v[142:143]
	v_cvt_f32_i32_e32 v137, v137
	v_cvt_f32_i32_e32 v136, v136
	v_cvt_f32_i32_e32 v131, v131
	v_cvt_f32_i32_e32 v130, v130
	v_or_b32_e32 v154, 0x100, v154
	v_lshl_add_u64 v[154:155], s[14:15], 0, v[154:155]
	s_lshl_b32 s22, s28, 2
	s_ashr_i32 s23, s22, 31
	s_lshl_b64 s[22:23], s[22:23], 2
	s_add_u32 s22, s48, s22
	s_addc_u32 s23, s49, s23
	s_waitcnt vmcnt(11)
; __device__ __forceinline__ unsigned cvt_pk_bf16(float lo, float hi) { unsigned r; asm volatile("v_cvt_pk_bf16_f32 %0, %1, %2" : "=v"(r) : "v"(lo), "v"(hi)); return r; }
;     __device__ __forceinline__ void operator()(const f32x4 (&acc)[2][2][4][2], const Unit& u, int wr, int wc, int fr, int fq) const {
;     ...
;             for (int m = 0; m < 4; ++m) { const size_t r = (size_t)(row0 + ai * HALF + m * 16); float ss = 0.f;
; #pragma unroll
;                 for (int bj = 0; bj < 2; ++bj) { const size_t off = r * 4096 + col0 + bj * HALF;
;                     const f32x4 v0 = acc[ai][bj][m][0] * scale + *(const f32x4*)(R + off), v1 = acc[ai][bj][m][1] * scale + *(const f32x4*)(R + off + 4);
;                     ss += (v0[0] * v0[0] + v0[1] * v0[1]) + (v0[2] * v0[2] + v0[3] * v0[3]) + (v1[0] * v1[0] + v1[1] * v1[1]) + (v1[2] * v1[2] + v1[3] * v1[3]);
;                     u32x4 w; w.x = cvt_pk_bf16(v0[0], v0[1]); w.y = cvt_pk_bf16(v0[2], v0[3]); w.z = cvt_pk_bf16(v1[0], v1[1]); w.w = cvt_pk_bf16(v1[2], v1[3]);
;                     *(u32x4*)(HB + off) = w;
;                     u32x2e q; q.x = q8x4(v0, gv[bj][0], (float)HQS); q.y = q8x4(v1, gv[bj][1], (float)HQS);
;                     *(u32x2e*)(Q8 + r * LDQ8 + col0 + bj * HALF) = q; }
;                 ss += __shfl_xor(ss, 16); ss += __shfl_xor(ss, 32);
;                 if (fq == 0) SSQP[r * 64 + u.pn * 4 + wc] = ss; }
	v_pk_fma_f32 v[160:161], v[160:161], s[26:27], v[148:149] op_sel_hi:[1,0,1]
	v_pk_fma_f32 v[158:159], v[158:159], s[26:27], v[146:147] op_sel_hi:[1,0,1]
	s_waitcnt vmcnt(10)
	v_pk_fma_f32 v[180:181], v[180:181], s[26:27], v[152:153] op_sel_hi:[1,0,1]
	v_pk_fma_f32 v[178:179], v[178:179], s[26:27], v[150:151] op_sel_hi:[1,0,1]
	v_cvt_pk_bf16_f32 v146, v158, v159
	v_cvt_pk_bf16_f32 v147, v160, v161
	s_waitcnt vmcnt(7)
	v_mul_f32_e32 v150, v74, v158
	v_cvt_pk_bf16_f32 v148, v178, v179
	v_cvt_pk_bf16_f32 v149, v180, v181
	v_mul_f32_e32 v151, v75, v159
	v_mul_f32_e32 v152, v76, v160
	v_mul_f32_e32 v153, v77, v161
	s_waitcnt vmcnt(6)
	v_mul_f32_e32 v184, v66, v178
	v_mul_f32_e32 v185, v67, v179
	v_mul_f32_e32 v186, v68, v180
	v_mul_f32_e32 v187, v69, v181
	global_store_dwordx4 v[182:183], v[146:149], off
	v_mul_f32_e32 v159, v159, v159
	v_mul_f32_e32 v161, v161, v161
	v_mul_f32_e32 v146, 0x41c00000, v150
	v_mul_f32_e32 v147, 0x41c00000, v151
	v_mul_f32_e32 v148, 0x41c00000, v152
	v_mul_f32_e32 v149, 0x41c00000, v153
	v_mul_f32_e32 v150, 0x41c00000, v184
	v_mul_f32_e32 v151, 0x41c00000, v185
	v_mul_f32_e32 v152, 0x41c00000, v186
	v_mul_f32_e32 v153, 0x41c00000, v187
	v_med3_f32 v146, v146, s51, v177
	v_med3_f32 v147, v147, s51, v177
	v_med3_f32 v148, v148, s51, v177
	v_med3_f32 v149, v149, s51, v177
	v_med3_f32 v150, v150, s51, v177
	v_med3_f32 v151, v151, s51, v177
	v_med3_f32 v152, v152, s51, v177
	v_med3_f32 v153, v153, s51, v177
	v_add_f32_e32 v146, 0x4b400000, v146
	v_add_f32_e32 v147, 0x4b400000, v147
	v_add_f32_e32 v148, 0x4b400000, v148
	v_add_f32_e32 v149, 0x4b400000, v149
	v_add_f32_e32 v150, 0x4b400000, v150
	v_add_f32_e32 v151, 0x4b400000, v151
	v_add_f32_e32 v152, 0x4b400000, v152
	v_add_f32_e32 v153, 0x4b400000, v153
	v_perm_b32 v146, v147, v146, s56
	v_perm_b32 v147, v149, v148, s57
	v_perm_b32 v148, v151, v150, s56
	v_perm_b32 v149, v153, v152, s57
	v_or_b32_e32 v146, v146, v147
	v_or_b32_e32 v147, v148, v149
	global_store_dwordx2 v[144:145], v[146:147], off
	s_nop 0
	s_nop 0
	s_nop 0
	v_cvt_f32_i32_e32 v157, v133
	v_cvt_f32_i32_e32 v156, v132
	v_and_b32_e32 v133, 64, v176
	v_mul_f32_e32 v179, v179, v179
	v_fmac_f32_e32 v159, v158, v158
	v_fmac_f32_e32 v161, v160, v160
	v_xor_b32_e32 v132, 16, v176
	v_add_u32_e32 v133, 64, v133
	v_mul_f32_e32 v181, v181, v181
	v_fmac_f32_e32 v179, v178, v178
	v_add_f32_e32 v158, v159, v161
	v_cmp_lt_i32_e32 vcc, v132, v133
	v_fmac_f32_e32 v181, v180, v180
	v_add_f32_e32 v158, v158, v179
	v_cndmask_b32_e32 v132, v176, v132, vcc
	v_add_f32_e32 v158, v181, v158
	v_lshlrev_b32_e32 v132, 2, v132
	v_xor_b32_e32 v182, 32, v176
	v_cmp_lt_i32_e32 vcc, v182, v133
	s_waitcnt vmcnt(6)
	v_pk_fma_f32 v[148:149], v[136:137], s[26:27], v[246:247] op_sel_hi:[1,0,1]
	v_pk_fma_f32 v[146:147], v[134:135], s[26:27], v[244:245] op_sel_hi:[1,0,1]
	s_waitcnt vmcnt(6)
	v_pk_fma_f32 v[130:131], v[130:131], s[26:27], v[248:249] op_sel_hi:[1,0,1]
	v_mul_f32_e32 v150, v147, v147
	v_mul_f32_e32 v151, v149, v149
	v_pk_fma_f32 v[152:153], v[156:157], s[26:27], v[250:251] op_sel_hi:[1,0,1]
	v_mul_f32_e32 v156, v131, v131
	v_cvt_pk_bf16_f32 v134, v146, v147
	v_cvt_pk_bf16_f32 v135, v148, v149
	v_cvt_pk_bf16_f32 v136, v130, v131
	v_mul_f32_e32 v131, v51, v131
	v_fmac_f32_e32 v150, v146, v146
	v_fmac_f32_e32 v151, v148, v148
	v_mul_f32_e32 v157, v153, v153
	v_mul_f32_e32 v160, v64, v148
	v_fmac_f32_e32 v156, v130, v130
	v_mul_f32_e32 v131, 0x41c00000, v131
	v_add_f32_e32 v148, v150, v151
	v_mul_f32_e32 v149, v65, v149
	v_fmac_f32_e32 v157, v152, v152
	v_med3_f32 v131, v131, s51, v177
	v_add_f32_e32 v148, v148, v156
	v_cvt_pk_bf16_f32 v137, v152, v153
	global_store_dwordx4 v[154:155], v[134:137], off
	v_mul_f32_e32 v159, v62, v146
	v_mul_f32_e32 v147, v63, v147
	v_mul_f32_e32 v136, 0x41c00000, v149
	v_add_f32_e32 v149, 0x4b400000, v131
	v_add_f32_e32 v131, v157, v148
	v_add_f32_e32 v131, v158, v131
	ds_bpermute_b32 v148, v132, v131
	v_mul_f32_e32 v161, v50, v130
	v_mul_f32_e32 v130, 0x41c00000, v159
	v_mul_f32_e32 v134, 0x41c00000, v147
	v_mul_f32_e32 v135, 0x41c00000, v160
	v_med3_f32 v130, v130, s51, v177
	v_med3_f32 v134, v134, s51, v177
	v_med3_f32 v135, v135, s51, v177
	v_med3_f32 v136, v136, s51, v177
	v_add_f32_e32 v130, 0x4b400000, v130
	v_add_f32_e32 v134, 0x4b400000, v134
	v_add_f32_e32 v135, 0x4b400000, v135
	v_add_f32_e32 v136, 0x4b400000, v136
	v_cndmask_b32_e32 v133, v176, v182, vcc
	v_perm_b32 v130, v134, v130, s56
	v_perm_b32 v134, v136, v135, s57
	v_mul_f32_e32 v178, v52, v152
	v_mul_f32_e32 v153, v53, v153
	v_or_b32_e32 v134, v130, v134
	s_waitcnt lgkmcnt(0)
	v_add_f32_e32 v130, v131, v148
	v_lshlrev_b32_e32 v133, 2, v133
	v_mul_f32_e32 v137, 0x41c00000, v161
	v_mul_f32_e32 v146, 0x41c00000, v178
	v_mul_f32_e32 v147, 0x41c00000, v153
	ds_bpermute_b32 v131, v133, v130
	v_med3_f32 v137, v137, s51, v177
	v_med3_f32 v146, v146, s51, v177
	v_med3_f32 v147, v147, s51, v177
	v_add_f32_e32 v137, 0x4b400000, v137
	v_add_f32_e32 v146, 0x4b400000, v146
	v_add_f32_e32 v147, 0x4b400000, v147
	v_perm_b32 v135, v149, v137, s56
	v_perm_b32 v136, v147, v146, s57
	v_or_b32_e32 v135, v135, v136
	global_store_dwordx2 v[144:145], v[134:135], off offset:128
	s_and_saveexec_b64 s[28:29], s[0:1]
	s_cbranch_execz .LBB0_619
	v_lshlrev_b64 v[134:135], 8, v[140:141]
	v_lshl_add_u64 v[134:135], s[22:23], 0, v[134:135]
	s_waitcnt lgkmcnt(0)
	v_add_f32_e32 v130, v130, v131
	global_store_dword v[134:135], v130, off
